# attention near-bucket bias path: the four key-list LDS reads of a step issued together with counted waits; on top of v24
# speedup vs baseline: 1.0106x; 1.0106x over previous
.LBB0_727:
	v_mov_b64_e32 v[176:177], v[172:173]
	v_mov_b64_e32 v[188:189], v[172:173]
	v_mov_b64_e32 v[192:193], v[172:173]
	s_lshl_b32 s51, s34, 6
	s_min_i32 s50, s42, 0xff
	s_andn2_b64 vcc, exec, s[12:13]
	v_mov_b64_e32 v[174:175], v[170:171]
	v_mov_b64_e32 v[186:187], v[170:171]
	v_mov_b64_e32 v[190:191], v[170:171]
	s_cbranch_vccnz .LBB0_736
	v_lshl_add_u32 v153, v210, 1, s43
	ds_read_b64 v[170:171], v153 offset:32768
	ds_read_b64 v[204:205], v153 offset:32800
	ds_read_b64 v[206:207], v153 offset:32832
	ds_read_b64 v[208:209], v153 offset:32864
	s_cmpk_lt_i32 s42, 0xff
	s_cselect_b64 s[12:13], -1, 0
	s_cmpk_gt_i32 s42, 0xfe
	s_waitcnt lgkmcnt(3)
	v_sub_u32_sdwa v0, s42, v170 dst_sel:DWORD dst_unused:UNUSED_PAD src0_sel:DWORD src1_sel:WORD_0
	v_sub_u32_sdwa v170, s42, v170 dst_sel:DWORD dst_unused:UNUSED_PAD src0_sel:DWORD src1_sel:WORD_1
	v_sub_u32_sdwa v172, s42, v171 dst_sel:DWORD dst_unused:UNUSED_PAD src0_sel:DWORD src1_sel:WORD_0
	v_min_i32_e32 v170, 0x7f, v170
	v_lshl_add_u32 v173, v170, 5, v234
	v_min_i32_e32 v170, 0x7f, v172
	v_min_i32_e32 v0, 0x7f, v0
	v_lshl_add_u32 v172, v170, 5, v234
	v_sub_u32_sdwa v170, s42, v171 dst_sel:DWORD dst_unused:UNUSED_PAD src0_sel:DWORD src1_sel:WORD_1
	v_lshl_add_u32 v0, v0, 5, v234
	v_min_i32_e32 v170, 0x7f, v170
	v_lshl_add_u32 v174, v170, 5, v234
	ds_read_b32 v170, v0
	ds_read_b32 v171, v173
	ds_read_b32 v172, v172
	ds_read_b32 v173, v174
	v_add_u32_e32 v0, s51, v210
	s_cbranch_scc1 .LBB0_730
	v_cmp_ge_i32_e32 vcc, s50, v0
	v_or_b32_e32 v174, 2, v0
	s_waitcnt lgkmcnt(3)
	v_cndmask_b32_e32 v170, v221, v170, vcc
	v_cmp_gt_i32_e32 vcc, s50, v0
	s_waitcnt lgkmcnt(2)
	s_nop 0
	v_cndmask_b32_e32 v171, v221, v171, vcc
	v_cmp_ge_i32_e32 vcc, s50, v174
	v_or_b32_e32 v174, 3, v0
	s_waitcnt lgkmcnt(1)
	v_cndmask_b32_e32 v172, v221, v172, vcc
	v_cmp_ge_i32_e32 vcc, s50, v174
	s_waitcnt lgkmcnt(0)
	s_nop 0
	v_cndmask_b32_e32 v173, v221, v173, vcc
.LBB0_730:
	s_andn2_b64 vcc, exec, s[12:13]
	s_waitcnt lgkmcnt(6)
	v_mov_b64_e32 v[174:175], v[204:205]
	v_sub_u32_sdwa v176, s42, v174 dst_sel:DWORD dst_unused:UNUSED_PAD src0_sel:DWORD src1_sel:WORD_0
	v_sub_u32_sdwa v174, s42, v174 dst_sel:DWORD dst_unused:UNUSED_PAD src0_sel:DWORD src1_sel:WORD_1
	v_sub_u32_sdwa v177, s42, v175 dst_sel:DWORD dst_unused:UNUSED_PAD src0_sel:DWORD src1_sel:WORD_0
	v_min_i32_e32 v174, 0x7f, v174
	v_lshl_add_u32 v178, v174, 5, v234
	v_min_i32_e32 v174, 0x7f, v177
	v_min_i32_e32 v176, 0x7f, v176
	v_lshl_add_u32 v177, v174, 5, v234
	v_sub_u32_sdwa v174, s42, v175 dst_sel:DWORD dst_unused:UNUSED_PAD src0_sel:DWORD src1_sel:WORD_1
	v_lshl_add_u32 v176, v176, 5, v234
	v_min_i32_e32 v174, 0x7f, v174
	v_lshl_add_u32 v179, v174, 5, v234
	ds_read_b32 v174, v176
	ds_read_b32 v175, v178
	ds_read_b32 v176, v177
	ds_read_b32 v177, v179
	v_cndmask_b32_e64 v178, 0, 1, s[12:13]
	v_cmp_ne_u32_e64 s[34:35], 1, v178
	s_cbranch_vccnz .LBB0_732
	v_add_u32_e32 v178, 16, v0
	v_cmp_ge_i32_e32 vcc, s50, v178
	v_add_u32_e32 v178, 17, v0
	s_waitcnt lgkmcnt(3)
	v_cndmask_b32_e32 v174, v221, v174, vcc
	v_cmp_ge_i32_e32 vcc, s50, v178
	v_add_u32_e32 v178, 18, v0
	s_waitcnt lgkmcnt(2)
	v_cndmask_b32_e32 v175, v221, v175, vcc
	v_cmp_ge_i32_e32 vcc, s50, v178
	v_add_u32_e32 v178, 19, v0
	s_waitcnt lgkmcnt(1)
	v_cndmask_b32_e32 v176, v221, v176, vcc
	v_cmp_ge_i32_e32 vcc, s50, v178
	s_waitcnt lgkmcnt(0)
	s_nop 0
	v_cndmask_b32_e32 v177, v221, v177, vcc
.LBB0_732:
	s_and_b64 vcc, exec, s[34:35]
	s_waitcnt lgkmcnt(9)
	v_mov_b64_e32 v[178:179], v[206:207]
	v_sub_u32_sdwa v180, s42, v178 dst_sel:DWORD dst_unused:UNUSED_PAD src0_sel:DWORD src1_sel:WORD_0
	v_sub_u32_sdwa v178, s42, v178 dst_sel:DWORD dst_unused:UNUSED_PAD src0_sel:DWORD src1_sel:WORD_1
	v_sub_u32_sdwa v181, s42, v179 dst_sel:DWORD dst_unused:UNUSED_PAD src0_sel:DWORD src1_sel:WORD_0
	v_min_i32_e32 v180, 0x7f, v180
	v_sub_u32_sdwa v179, s42, v179 dst_sel:DWORD dst_unused:UNUSED_PAD src0_sel:DWORD src1_sel:WORD_1
	v_min_i32_e32 v178, 0x7f, v178
	v_lshl_add_u32 v180, v180, 5, v234
	v_min_i32_e32 v181, 0x7f, v181
	v_min_i32_e32 v179, 0x7f, v179
	v_lshl_add_u32 v178, v178, 5, v234
	v_lshl_add_u32 v181, v181, 5, v234
	v_lshl_add_u32 v179, v179, 5, v234
	ds_read_b32 v186, v180
	ds_read_b32 v187, v178
	ds_read_b32 v188, v181
	ds_read_b32 v189, v179
	s_cbranch_vccnz .LBB0_734
	v_add_u32_e32 v178, 32, v0
	v_cmp_ge_i32_e32 vcc, s50, v178
	v_add_u32_e32 v178, 33, v0
	s_waitcnt lgkmcnt(3)
	v_cndmask_b32_e32 v186, v221, v186, vcc
	v_cmp_ge_i32_e32 vcc, s50, v178
	v_add_u32_e32 v178, 34, v0
	s_waitcnt lgkmcnt(2)
	v_cndmask_b32_e32 v187, v221, v187, vcc
	v_cmp_ge_i32_e32 vcc, s50, v178
	v_add_u32_e32 v178, 35, v0
	s_waitcnt lgkmcnt(1)
	v_cndmask_b32_e32 v188, v221, v188, vcc
	v_cmp_ge_i32_e32 vcc, s50, v178
	s_waitcnt lgkmcnt(0)
	s_nop 0
	v_cndmask_b32_e32 v189, v221, v189, vcc
.LBB0_734:
	s_and_b64 vcc, exec, s[34:35]
	s_waitcnt lgkmcnt(12)
	v_mov_b64_e32 v[178:179], v[208:209]
	v_sub_u32_sdwa v153, s42, v178 dst_sel:DWORD dst_unused:UNUSED_PAD src0_sel:DWORD src1_sel:WORD_0
	v_sub_u32_sdwa v178, s42, v178 dst_sel:DWORD dst_unused:UNUSED_PAD src0_sel:DWORD src1_sel:WORD_1
	v_sub_u32_sdwa v180, s42, v179 dst_sel:DWORD dst_unused:UNUSED_PAD src0_sel:DWORD src1_sel:WORD_0
	v_min_i32_e32 v153, 0x7f, v153
	v_sub_u32_sdwa v179, s42, v179 dst_sel:DWORD dst_unused:UNUSED_PAD src0_sel:DWORD src1_sel:WORD_1
	v_min_i32_e32 v178, 0x7f, v178
	v_lshl_add_u32 v153, v153, 5, v234
	v_min_i32_e32 v180, 0x7f, v180
	v_min_i32_e32 v179, 0x7f, v179
	v_lshl_add_u32 v178, v178, 5, v234
	v_lshl_add_u32 v180, v180, 5, v234
	v_lshl_add_u32 v179, v179, 5, v234
	ds_read_b32 v190, v153
	ds_read_b32 v191, v178
	ds_read_b32 v192, v180
	ds_read_b32 v193, v179
	s_cbranch_vccnz .LBB0_736
	v_add_u32_e32 v153, 48, v0
	v_cmp_ge_i32_e32 vcc, s50, v153
	v_add_u32_e32 v153, 49, v0
	s_waitcnt lgkmcnt(3)
	v_cndmask_b32_e32 v190, v221, v190, vcc
	v_cmp_ge_i32_e32 vcc, s50, v153
	v_add_u32_e32 v153, 50, v0
	v_add_u32_e32 v0, 51, v0
	s_waitcnt lgkmcnt(2)
	v_cndmask_b32_e32 v191, v221, v191, vcc
	v_cmp_ge_i32_e32 vcc, s50, v153
	s_waitcnt lgkmcnt(1)
	s_nop 0
	v_cndmask_b32_e32 v192, v221, v192, vcc
	v_cmp_ge_i32_e32 vcc, s50, v0
	s_waitcnt lgkmcnt(0)
	s_nop 0
	v_cndmask_b32_e32 v193, v221, v193, vcc

.LBB0_751:
	v_mov_b64_e32 v[172:173], v[152:153]
	v_mov_b64_e32 v[176:177], v[152:153]
	v_mov_b64_e32 v[180:181], v[152:153]
	s_andn2_b64 vcc, exec, s[12:13]
	v_mov_b64_e32 v[170:171], v[150:151]
	v_mov_b64_e32 v[174:175], v[150:151]
	v_mov_b64_e32 v[178:179], v[150:151]
	s_cbranch_vccnz .LBB0_760
	v_lshl_add_u32 v178, v210, 1, s43
	ds_read_b64 v[150:151], v178 offset:32896
	ds_read_b64 v[204:205], v178 offset:32928
	ds_read_b64 v[206:207], v178 offset:32960
	ds_read_b64 v[208:209], v178 offset:32992
	s_cmpk_lt_i32 s42, 0xff
	s_cselect_b64 s[12:13], -1, 0
	s_cmpk_gt_i32 s42, 0xfe
	s_waitcnt lgkmcnt(3)
	v_sub_u32_sdwa v0, s42, v150 dst_sel:DWORD dst_unused:UNUSED_PAD src0_sel:DWORD src1_sel:WORD_0
	v_sub_u32_sdwa v150, s42, v150 dst_sel:DWORD dst_unused:UNUSED_PAD src0_sel:DWORD src1_sel:WORD_1
	v_sub_u32_sdwa v152, s42, v151 dst_sel:DWORD dst_unused:UNUSED_PAD src0_sel:DWORD src1_sel:WORD_0
	v_min_i32_e32 v150, 0x7f, v150
	v_lshl_add_u32 v153, v150, 5, v234
	v_min_i32_e32 v150, 0x7f, v152
	v_min_i32_e32 v0, 0x7f, v0
	v_lshl_add_u32 v152, v150, 5, v234
	v_sub_u32_sdwa v150, s42, v151 dst_sel:DWORD dst_unused:UNUSED_PAD src0_sel:DWORD src1_sel:WORD_1
	v_lshl_add_u32 v0, v0, 5, v234
	v_min_i32_e32 v150, 0x7f, v150
	v_lshl_add_u32 v170, v150, 5, v234
	ds_read_b32 v150, v0
	ds_read_b32 v151, v153
	ds_read_b32 v152, v152
	ds_read_b32 v153, v170
	v_add3_u32 v0, v210, s51, 64
	s_cbranch_scc1 .LBB0_754
	v_cmp_ge_i32_e32 vcc, s50, v0
	v_or_b32_e32 v170, 2, v0
	s_waitcnt lgkmcnt(3)
	v_cndmask_b32_e32 v150, v221, v150, vcc
	v_cmp_gt_i32_e32 vcc, s50, v0
	s_waitcnt lgkmcnt(2)
	s_nop 0
	v_cndmask_b32_e32 v151, v221, v151, vcc
	v_cmp_ge_i32_e32 vcc, s50, v170
	v_or_b32_e32 v170, 3, v0
	s_waitcnt lgkmcnt(1)
	v_cndmask_b32_e32 v152, v221, v152, vcc
	v_cmp_ge_i32_e32 vcc, s50, v170
	s_waitcnt lgkmcnt(0)
	s_nop 0
	v_cndmask_b32_e32 v153, v221, v153, vcc
.LBB0_754:
	s_andn2_b64 vcc, exec, s[12:13]
	s_waitcnt lgkmcnt(6)
	v_mov_b64_e32 v[170:171], v[204:205]
	v_sub_u32_sdwa v172, s42, v170 dst_sel:DWORD dst_unused:UNUSED_PAD src0_sel:DWORD src1_sel:WORD_0
	v_sub_u32_sdwa v170, s42, v170 dst_sel:DWORD dst_unused:UNUSED_PAD src0_sel:DWORD src1_sel:WORD_1
	v_sub_u32_sdwa v173, s42, v171 dst_sel:DWORD dst_unused:UNUSED_PAD src0_sel:DWORD src1_sel:WORD_0
	v_min_i32_e32 v170, 0x7f, v170
	v_lshl_add_u32 v174, v170, 5, v234
	v_min_i32_e32 v170, 0x7f, v173
	v_min_i32_e32 v172, 0x7f, v172
	v_lshl_add_u32 v173, v170, 5, v234
	v_sub_u32_sdwa v170, s42, v171 dst_sel:DWORD dst_unused:UNUSED_PAD src0_sel:DWORD src1_sel:WORD_1
	v_lshl_add_u32 v172, v172, 5, v234
	v_min_i32_e32 v170, 0x7f, v170
	v_lshl_add_u32 v175, v170, 5, v234
	ds_read_b32 v170, v172
	ds_read_b32 v171, v174
	ds_read_b32 v172, v173
	ds_read_b32 v173, v175
	v_cndmask_b32_e64 v174, 0, 1, s[12:13]
	v_cmp_ne_u32_e64 s[34:35], 1, v174
	s_cbranch_vccnz .LBB0_756
	v_add_u32_e32 v174, 16, v0
	v_cmp_ge_i32_e32 vcc, s50, v174
	v_add_u32_e32 v174, 17, v0
	s_waitcnt lgkmcnt(3)
	v_cndmask_b32_e32 v170, v221, v170, vcc
	v_cmp_ge_i32_e32 vcc, s50, v174
	v_add_u32_e32 v174, 18, v0
	s_waitcnt lgkmcnt(2)
	v_cndmask_b32_e32 v171, v221, v171, vcc
	v_cmp_ge_i32_e32 vcc, s50, v174
	v_add_u32_e32 v174, 19, v0
	s_waitcnt lgkmcnt(1)
	v_cndmask_b32_e32 v172, v221, v172, vcc
	v_cmp_ge_i32_e32 vcc, s50, v174
	s_waitcnt lgkmcnt(0)
	s_nop 0
	v_cndmask_b32_e32 v173, v221, v173, vcc
.LBB0_756:
	s_and_b64 vcc, exec, s[34:35]
	s_waitcnt lgkmcnt(9)
	v_mov_b64_e32 v[174:175], v[206:207]
	v_sub_u32_sdwa v176, s42, v174 dst_sel:DWORD dst_unused:UNUSED_PAD src0_sel:DWORD src1_sel:WORD_0
	v_sub_u32_sdwa v174, s42, v174 dst_sel:DWORD dst_unused:UNUSED_PAD src0_sel:DWORD src1_sel:WORD_1
	v_sub_u32_sdwa v177, s42, v175 dst_sel:DWORD dst_unused:UNUSED_PAD src0_sel:DWORD src1_sel:WORD_0
	v_min_i32_e32 v174, 0x7f, v174
	v_lshl_add_u32 v179, v174, 5, v234
	v_min_i32_e32 v174, 0x7f, v177
	v_min_i32_e32 v176, 0x7f, v176
	v_lshl_add_u32 v177, v174, 5, v234
	v_sub_u32_sdwa v174, s42, v175 dst_sel:DWORD dst_unused:UNUSED_PAD src0_sel:DWORD src1_sel:WORD_1
	v_lshl_add_u32 v176, v176, 5, v234
	v_min_i32_e32 v174, 0x7f, v174
	v_lshl_add_u32 v180, v174, 5, v234
	ds_read_b32 v174, v176
	ds_read_b32 v175, v179
	ds_read_b32 v176, v177
	ds_read_b32 v177, v180
	s_cbranch_vccnz .LBB0_758
	v_add_u32_e32 v179, 32, v0
	v_cmp_ge_i32_e32 vcc, s50, v179
	v_add_u32_e32 v179, 33, v0
	s_waitcnt lgkmcnt(3)
	v_cndmask_b32_e32 v174, v221, v174, vcc
	v_cmp_ge_i32_e32 vcc, s50, v179
	v_add_u32_e32 v179, 34, v0
	s_waitcnt lgkmcnt(2)
	v_cndmask_b32_e32 v175, v221, v175, vcc
	v_cmp_ge_i32_e32 vcc, s50, v179
	v_add_u32_e32 v179, 35, v0
	s_waitcnt lgkmcnt(1)
	v_cndmask_b32_e32 v176, v221, v176, vcc
	v_cmp_ge_i32_e32 vcc, s50, v179
	s_waitcnt lgkmcnt(0)
	s_nop 0
	v_cndmask_b32_e32 v177, v221, v177, vcc
.LBB0_758:
	s_and_b64 vcc, exec, s[34:35]
	s_waitcnt lgkmcnt(12)
	v_mov_b64_e32 v[178:179], v[208:209]
	v_sub_u32_sdwa v180, s42, v178 dst_sel:DWORD dst_unused:UNUSED_PAD src0_sel:DWORD src1_sel:WORD_0
	v_sub_u32_sdwa v178, s42, v178 dst_sel:DWORD dst_unused:UNUSED_PAD src0_sel:DWORD src1_sel:WORD_1
	v_sub_u32_sdwa v181, s42, v179 dst_sel:DWORD dst_unused:UNUSED_PAD src0_sel:DWORD src1_sel:WORD_0
	v_min_i32_e32 v178, 0x7f, v178
	v_lshl_add_u32 v184, v178, 5, v234
	v_min_i32_e32 v178, 0x7f, v181
	v_min_i32_e32 v180, 0x7f, v180
	v_lshl_add_u32 v181, v178, 5, v234
	v_sub_u32_sdwa v178, s42, v179 dst_sel:DWORD dst_unused:UNUSED_PAD src0_sel:DWORD src1_sel:WORD_1
	v_lshl_add_u32 v180, v180, 5, v234
	v_min_i32_e32 v178, 0x7f, v178
	v_lshl_add_u32 v185, v178, 5, v234
	ds_read_b32 v178, v180
	ds_read_b32 v179, v184
	ds_read_b32 v180, v181
	ds_read_b32 v181, v185
	s_cbranch_vccnz .LBB0_760
	v_add_u32_e32 v184, 48, v0
	v_cmp_ge_i32_e32 vcc, s50, v184
	v_add_u32_e32 v184, 49, v0
	s_waitcnt lgkmcnt(3)
	v_cndmask_b32_e32 v178, v221, v178, vcc
	v_cmp_ge_i32_e32 vcc, s50, v184
	v_add_u32_e32 v184, 50, v0
	v_add_u32_e32 v0, 51, v0
	s_waitcnt lgkmcnt(2)
	v_cndmask_b32_e32 v179, v221, v179, vcc
	v_cmp_ge_i32_e32 vcc, s50, v184
	s_waitcnt lgkmcnt(1)
	s_nop 0
	v_cndmask_b32_e32 v180, v221, v180, vcc
	v_cmp_ge_i32_e32 vcc, s50, v0
	s_waitcnt lgkmcnt(0)
	s_nop 0
	v_cndmask_b32_e32 v181, v221, v181, vcc
